# speedup vs baseline: 1.0377x; 1.0377x over previous
.Lh_rows_done:
	v_bfe_u32 v45, v1, 1, 3
	v_lshlrev_b32_e32 v45, 4, v45
	v_xor_b32_e32 v46, 16, v45
	v_xor_b32_e32 v47, 32, v45
	v_xor_b32_e32 v48, 48, v45
	v_xor_b32_e32 v50, 64, v45
	v_xor_b32_e32 v51, 80, v45
	v_xor_b32_e32 v52, 96, v45
	v_xor_b32_e32 v53, 112, v45
	v_add_u32_e32 v45, v44, v45
	v_add_u32_e32 v46, v44, v46
	v_add_u32_e32 v47, v44, v47
	v_add_u32_e32 v48, v44, v48
	v_add_u32_e32 v50, v44, v50
	v_add_u32_e32 v51, v44, v51
	v_add_u32_e32 v52, v44, v52
	v_add_u32_e32 v53, v44, v53
	v_add_u32_e32 v54, 6, v1
	v_and_b32_e32 v54, 63, v54
	v_lshlrev_b32_e32 v54, 2, v54
	s_mul_i32 s58, s2, 0x600
	s_add_u32 s10, s10, s58
	s_addc_u32 s11, s11, 0
	s_lshl_b32 s59, s3, 8
	s_cmp_lt_u32 s3, 6
	s_cselect_b32 s59, s59, 0
	v_add_u32_e32 v49, s59, v49
	s_lshl_b32 s58, s2, 2
	s_add_u32 s12, s12, s58
	s_addc_u32 s13, s13, 0
	s_setprio 3
	s_cmp_lt_u32 s3, 8
	s_cbranch_scc1 .Lh_nostagger
	s_sleep 3

amdhsa.kernels:
  - .agpr_count:     0
    .args:
      - .actual_access:  read_only
        .address_space:  global
        .offset:         0
        .size:           8
        .value_kind:     global_buffer
      - .actual_access:  read_only
        .address_space:  global
        .offset:         8
        .size:           8
        .value_kind:     global_buffer
      - .actual_access:  read_only
        .address_space:  global
        .offset:         16
        .size:           8
        .value_kind:     global_buffer
      - .actual_access:  write_only
        .address_space:  global
        .offset:         24
        .size:           8
        .value_kind:     global_buffer
      - .actual_access:  write_only
        .address_space:  global
        .offset:         32
        .size:           8
        .value_kind:     global_buffer
      - .actual_access:  write_only
        .address_space:  global
        .offset:         40
        .size:           8
        .value_kind:     global_buffer
    .group_segment_fixed_size: 34048
    .kernarg_segment_align: 8
    .kernarg_segment_size: 48
    .language:       OpenCL C
    .language_version:
      - 2
      - 0
    .max_flat_workgroup_size: 1024
    .name:           _Z6k_histPKfS0_S0_PfPiS1_
    .private_segment_fixed_size: 0
    .sgpr_count:     66
    .sgpr_spill_count: 0
    .symbol:         _Z6k_histPKfS0_S0_PfPiS1_.kd
    .uniform_work_group_size: 1
    .uses_dynamic_stack: false
    .vgpr_count:     88
    .vgpr_spill_count: 0
    .wavefront_size: 64
  - .agpr_count:     0
    .args:
      - .actual_access:  read_only
        .address_space:  global
        .offset:         0
        .size:           8
        .value_kind:     global_buffer
      - .actual_access:  read_only
        .address_space:  global
        .offset:         8
        .size:           8
        .value_kind:     global_buffer
      - .address_space:  global
        .offset:         16
        .size:           8
        .value_kind:     global_buffer
    .group_segment_fixed_size: 2080
    .kernarg_segment_align: 8
    .kernarg_segment_size: 24
    .language:       OpenCL C
    .language_version:
      - 2
      - 0
    .max_flat_workgroup_size: 256
    .name:           _Z7k_finalPKfPKiPf
    .private_segment_fixed_size: 0
    .sgpr_count:     34
    .sgpr_spill_count: 0
    .symbol:         _Z7k_finalPKfPKiPf.kd
    .uniform_work_group_size: 1
    .uses_dynamic_stack: false
    .vgpr_count:     36
    .vgpr_spill_count: 0
    .wavefront_size: 64
